# k_bhist packing blocks: two dummy s_loads warm the scalar cache with kernarg lines 1 and 2 at the start of the packing path
# speedup vs baseline: 1.0141x; 1.0000x over previous
.LBB2_20:
	s_and_b64 vcc, exec, s[4:5]
	s_cbranch_vccz .LBB2_66
	s_load_dword s19, s[0:1], 0x40
	s_load_dword s20, s[0:1], 0x80
	s_lshl_b32 s16, s2, 10
	s_add_i32 s2, s16, 0xfffc0000
	v_or_b32_e32 v2, s2, v0
	v_xor_b32_e32 v2, 0xfc00, v2
	s_movk_i32 s2, 0x1000
	v_cmp_gt_i32_e32 vcc, s2, v2
	v_or_b32_e32 v5, s16, v0
	v_xor_b32_e32 v5, 0xfc00, v5
	v_and_b32_e32 v4, 7, v0
	s_and_saveexec_b64 s[2:3], vcc
	s_cbranch_execz .LBB2_29
	s_load_dwordx2 s[6:7], s[0:1], 0x60
	s_load_dwordx2 s[4:5], s[0:1], 0x18
	v_max_i32_e32 v1, 0xffff1000, v2
	v_sub_u32_e32 v1, v1, v5
	v_add_u32_e32 v1, 0x4ffff, v1
	s_mov_b32 s8, 0xffff
	v_cmp_lt_u32_e32 vcc, s8, v1
	s_mov_b64 s[10:11], -1
	v_mov_b32_e32 v6, v2
	s_and_saveexec_b64 s[8:9], vcc
	s_cbranch_execz .LBB2_26
	v_mov_b32_e32 v3, 1
	v_add_u32_sdwa v8, v1, v3 dst_sel:DWORD dst_unused:UNUSED_PAD src0_sel:WORD_1 src1_sel:DWORD
	v_and_b32_e32 v9, 0x1fffe, v8
	v_add_u32_e32 v3, 0x10000, v2
	v_mov_b32_e32 v1, v4
	s_mov_b64 s[10:11], 0
	v_mov_b32_e32 v10, v9
	v_mov_b64_e32 v[6:7], v[2:3]

	.amdhsa_kernel _Z7k_bhistPKiPiPfPKfS4_PDF16_S4_S4_S4_S4_S4_S4_S5_S5_S5_S5_S2_
		.amdhsa_group_segment_fixed_size 628
		.amdhsa_private_segment_fixed_size 0
		.amdhsa_kernarg_size 136
		.amdhsa_user_sgpr_count 2
		.amdhsa_user_sgpr_dispatch_ptr 0
		.amdhsa_user_sgpr_queue_ptr 0
		.amdhsa_user_sgpr_kernarg_segment_ptr 1
		.amdhsa_user_sgpr_dispatch_id 0
		.amdhsa_user_sgpr_kernarg_preload_length 0
		.amdhsa_user_sgpr_kernarg_preload_offset 0
		.amdhsa_user_sgpr_private_segment_size 0
		.amdhsa_uses_dynamic_stack 0
		.amdhsa_enable_private_segment 0
		.amdhsa_system_sgpr_workgroup_id_x 1
		.amdhsa_system_sgpr_workgroup_id_y 0
		.amdhsa_system_sgpr_workgroup_id_z 0
		.amdhsa_system_sgpr_workgroup_info 0
		.amdhsa_system_vgpr_workitem_id 0
		.amdhsa_next_free_vgpr 32
		.amdhsa_next_free_sgpr 21
		.amdhsa_accum_offset 32
		.amdhsa_reserve_vcc 1
		.amdhsa_float_round_mode_32 0
		.amdhsa_float_round_mode_16_64 0
		.amdhsa_float_denorm_mode_32 3
		.amdhsa_float_denorm_mode_16_64 3
		.amdhsa_dx10_clamp 1
		.amdhsa_ieee_mode 1
		.amdhsa_fp16_overflow 0
		.amdhsa_tg_split 0
		.amdhsa_exception_fp_ieee_invalid_op 0
		.amdhsa_exception_fp_denorm_src 0
		.amdhsa_exception_fp_ieee_div_zero 0
		.amdhsa_exception_fp_ieee_overflow 0
		.amdhsa_exception_fp_ieee_underflow 0
		.amdhsa_exception_fp_ieee_inexact 0
		.amdhsa_exception_int_div_zero 0
	.end_amdhsa_kernel

amdhsa.kernels:
  - .agpr_count:     0
    .args:
      - .actual_access:  read_only
        .address_space:  global
        .offset:         0
        .size:           8
        .value_kind:     global_buffer
      - .actual_access:  read_only
        .address_space:  global
        .offset:         8
        .size:           8
        .value_kind:     global_buffer
      - .actual_access:  read_only
        .address_space:  global
        .offset:         16
        .size:           8
        .value_kind:     global_buffer
      - .actual_access:  read_only
        .address_space:  global
        .offset:         24
        .size:           8
        .value_kind:     global_buffer
      - .actual_access:  write_only
        .address_space:  global
        .offset:         32
        .size:           8
        .value_kind:     global_buffer
      - .actual_access:  write_only
        .address_space:  global
        .offset:         40
        .size:           8
        .value_kind:     global_buffer
    .group_segment_fixed_size: 56512
    .kernarg_segment_align: 8
    .kernarg_segment_size: 48
    .language:       OpenCL C
    .language_version:
      - 2
      - 0
    .max_flat_workgroup_size: 1024
    .name:           _Z10k_bscatterPKiS0_PKfS0_PiP15HIP_vector_typeIiLj2EE
    .private_segment_fixed_size: 0
    .sgpr_count:     42
    .sgpr_spill_count: 0
    .symbol:         _Z10k_bscatterPKiS0_PKfS0_PiP15HIP_vector_typeIiLj2EE.kd
    .uniform_work_group_size: 1
    .uses_dynamic_stack: false
    .vgpr_count:     89
    .vgpr_spill_count: 0
    .wavefront_size: 64
  - .agpr_count:     0
    .args:
      - .actual_access:  read_only
        .address_space:  global
        .offset:         0
        .size:           8
        .value_kind:     global_buffer
      - .actual_access:  read_only
        .address_space:  global
        .offset:         8
        .size:           8
        .value_kind:     global_buffer
      - .actual_access:  write_only
        .address_space:  global
        .offset:         16
        .size:           8
        .value_kind:     global_buffer
      - .actual_access:  write_only
        .address_space:  global
        .offset:         24
        .size:           8
        .value_kind:     global_buffer
      - .actual_access:  write_only
        .address_space:  global
        .offset:         32
        .size:           8
        .value_kind:     global_buffer
      - .actual_access:  write_only
        .address_space:  global
        .offset:         40
        .size:           8
        .value_kind:     global_buffer
      - .actual_access:  read_only
        .address_space:  global
        .offset:         48
        .size:           8
        .value_kind:     global_buffer
      - .actual_access:  write_only
        .address_space:  global
        .offset:         56
        .size:           8
        .value_kind:     global_buffer
    .group_segment_fixed_size: 12352
    .kernarg_segment_align: 8
    .kernarg_segment_size: 64
    .language:       OpenCL C
    .language_version:
      - 2
      - 0
    .max_flat_workgroup_size: 1024
    .name:           _Z8k_bfinalPK15HIP_vector_typeIiLj2EEPKiPS0_PiS6_PfPKfPDF16_
    .private_segment_fixed_size: 0
    .sgpr_count:     38
    .sgpr_spill_count: 0
    .symbol:         _Z8k_bfinalPK15HIP_vector_typeIiLj2EEPKiPS0_PiS6_PfPKfPDF16_.kd
    .uniform_work_group_size: 1
    .uses_dynamic_stack: false
    .vgpr_count:     72
    .vgpr_spill_count: 0
    .wavefront_size: 64
  - .agpr_count:     0
    .args:
      - .actual_access:  read_only
        .address_space:  global
        .offset:         0
        .size:           8
        .value_kind:     global_buffer
      - .actual_access:  write_only
        .address_space:  global
        .offset:         8
        .size:           8
        .value_kind:     global_buffer
      - .actual_access:  write_only
        .address_space:  global
        .offset:         16
        .size:           8
        .value_kind:     global_buffer
      - .actual_access:  read_only
        .address_space:  global
        .offset:         24
        .size:           8
        .value_kind:     global_buffer
      - .actual_access:  read_only
        .address_space:  global
        .offset:         32
        .size:           8
        .value_kind:     global_buffer
      - .actual_access:  write_only
        .address_space:  global
        .offset:         40
        .size:           8
        .value_kind:     global_buffer
      - .actual_access:  read_only
        .address_space:  global
        .offset:         48
        .size:           8
        .value_kind:     global_buffer
      - .actual_access:  read_only
        .address_space:  global
        .offset:         56
        .size:           8
        .value_kind:     global_buffer
      - .actual_access:  read_only
        .address_space:  global
        .offset:         64
        .size:           8
        .value_kind:     global_buffer
      - .actual_access:  read_only
        .address_space:  global
        .offset:         72
        .size:           8
        .value_kind:     global_buffer
      - .actual_access:  read_only
        .address_space:  global
        .offset:         80
        .size:           8
        .value_kind:     global_buffer
      - .actual_access:  read_only
        .address_space:  global
        .offset:         88
        .size:           8
        .value_kind:     global_buffer
      - .actual_access:  write_only
        .address_space:  global
        .offset:         96
        .size:           8
        .value_kind:     global_buffer
      - .actual_access:  write_only
        .address_space:  global
        .offset:         104
        .size:           8
        .value_kind:     global_buffer
      - .actual_access:  write_only
        .address_space:  global
        .offset:         112
        .size:           8
        .value_kind:     global_buffer
      - .actual_access:  write_only
        .address_space:  global
        .offset:         120
        .size:           8
        .value_kind:     global_buffer
      - .actual_access:  write_only
        .address_space:  global
        .offset:         128
        .size:           8
        .value_kind:     global_buffer
    .group_segment_fixed_size: 628
    .kernarg_segment_align: 8
    .kernarg_segment_size: 136
    .language:       OpenCL C
    .language_version:
      - 2
      - 0
    .max_flat_workgroup_size: 1024
    .name:           _Z7k_bhistPKiPiPfPKfS4_PDF16_S4_S4_S4_S4_S4_S4_S5_S5_S5_S5_S2_
    .private_segment_fixed_size: 0
    .sgpr_count:     27
    .sgpr_spill_count: 0
    .symbol:         _Z7k_bhistPKiPiPfPKfS4_PDF16_S4_S4_S4_S4_S4_S4_S5_S5_S5_S5_S2_.kd
    .uniform_work_group_size: 1
    .uses_dynamic_stack: false
    .vgpr_count:     32
    .vgpr_spill_count: 0
    .wavefront_size: 64
  - .agpr_count:     0
    .args:
      - .actual_access:  read_only
        .address_space:  global
        .offset:         0
        .size:           8
        .value_kind:     global_buffer
      - .actual_access:  read_only
        .address_space:  global
        .offset:         8
        .size:           8
        .value_kind:     global_buffer
      - .actual_access:  read_only
        .address_space:  global
        .offset:         16
        .size:           8
        .value_kind:     global_buffer
      - .actual_access:  read_only
        .address_space:  global
        .offset:         24
        .size:           8
        .value_kind:     global_buffer
      - .actual_access:  read_only
        .address_space:  global
        .offset:         32
        .size:           8
        .value_kind:     global_buffer
      - .actual_access:  read_only
        .address_space:  global
        .offset:         40
        .size:           8
        .value_kind:     global_buffer
      - .actual_access:  read_only
        .address_space:  global
        .offset:         48
        .size:           8
        .value_kind:     global_buffer
      - .actual_access:  read_only
        .address_space:  global
        .offset:         56
        .size:           8
        .value_kind:     global_buffer
      - .actual_access:  read_only
        .address_space:  global
        .offset:         64
        .size:           8
        .value_kind:     global_buffer
      - .actual_access:  write_only
        .address_space:  global
        .offset:         72
        .size:           8
        .value_kind:     global_buffer
      - .actual_access:  write_only
        .address_space:  global
        .offset:         80
        .size:           8
        .value_kind:     global_buffer
      - .offset:         88
        .size:           4
        .value_kind:     hidden_block_count_x
      - .offset:         92
        .size:           4
        .value_kind:     hidden_block_count_y
      - .offset:         96
        .size:           4
        .value_kind:     hidden_block_count_z
      - .offset:         100
        .size:           2
        .value_kind:     hidden_group_size_x
      - .offset:         102
        .size:           2
        .value_kind:     hidden_group_size_y
      - .offset:         104
        .size:           2
        .value_kind:     hidden_group_size_z
      - .offset:         106
        .size:           2
        .value_kind:     hidden_remainder_x
      - .offset:         108
        .size:           2
        .value_kind:     hidden_remainder_y
      - .offset:         110
        .size:           2
        .value_kind:     hidden_remainder_z
      - .offset:         128
        .size:           8
        .value_kind:     hidden_global_offset_x
      - .offset:         136
        .size:           8
        .value_kind:     hidden_global_offset_y
      - .offset:         144
        .size:           8
        .value_kind:     hidden_global_offset_z
      - .offset:         152
        .size:           2
        .value_kind:     hidden_grid_dims
    .group_segment_fixed_size: 2048
    .kernarg_segment_align: 8
    .kernarg_segment_size: 344
    .language:       OpenCL C
    .language_version:
      - 2
      - 0
    .max_flat_workgroup_size: 256
    .name:           _Z7k_fold2PKfS0_S0_S0_S0_S0_S0_S0_S0_PDF16_Pf
    .private_segment_fixed_size: 0
    .sgpr_count:     44
    .sgpr_spill_count: 0
    .symbol:         _Z7k_fold2PKfS0_S0_S0_S0_S0_S0_S0_S0_PDF16_Pf.kd
    .uniform_work_group_size: 1
    .uses_dynamic_stack: false
    .vgpr_count:     61
    .vgpr_spill_count: 0
    .wavefront_size: 64
  - .agpr_count:     0
    .args:
      - .actual_access:  read_only
        .address_space:  global
        .offset:         0
        .size:           8
        .value_kind:     global_buffer
      - .actual_access:  read_only
        .address_space:  global
        .offset:         8
        .size:           8
        .value_kind:     global_buffer
      - .actual_access:  write_only
        .address_space:  global
        .offset:         16
        .size:           8
        .value_kind:     global_buffer
      - .actual_access:  read_only
        .address_space:  global
        .offset:         24
        .size:           8
        .value_kind:     global_buffer
      - .actual_access:  read_only
        .address_space:  global
        .offset:         32
        .size:           8
        .value_kind:     global_buffer
      - .actual_access:  read_only
        .address_space:  global
        .offset:         40
        .size:           8
        .value_kind:     global_buffer
      - .actual_access:  read_only
        .address_space:  global
        .offset:         48
        .size:           8
        .value_kind:     global_buffer
      - .actual_access:  read_only
        .address_space:  global
        .offset:         56
        .size:           8
        .value_kind:     global_buffer
      - .actual_access:  read_only
        .address_space:  global
        .offset:         64
        .size:           8
        .value_kind:     global_buffer
      - .actual_access:  read_only
        .address_space:  global
        .offset:         72
        .size:           8
        .value_kind:     global_buffer
      - .actual_access:  read_only
        .address_space:  global
        .offset:         80
        .size:           8
        .value_kind:     global_buffer
      - .actual_access:  write_only
        .address_space:  global
        .offset:         88
        .size:           8
        .value_kind:     global_buffer
      - .actual_access:  write_only
        .address_space:  global
        .offset:         96
        .size:           8
        .value_kind:     global_buffer
      - .address_space:  global
        .offset:         104
        .size:           8
        .value_kind:     global_buffer
      - .actual_access:  write_only
        .address_space:  global
        .offset:         112
        .size:           8
        .value_kind:     global_buffer
      - .actual_access:  read_only
        .address_space:  global
        .offset:         120
        .size:           8
        .value_kind:     global_buffer
      - .actual_access:  read_only
        .address_space:  global
        .offset:         128
        .size:           8
        .value_kind:     global_buffer
    .group_segment_fixed_size: 22272
    .kernarg_segment_align: 8
    .kernarg_segment_size: 136
    .language:       OpenCL C
    .language_version:
      - 2
      - 0
    .max_flat_workgroup_size: 256
    .name:           _Z5k_gcnILi1EEvPKvPK15HIP_vector_typeIiLj2EEPfPKiS8_PKfPKDF16_SA_SA_SA_SA_S6_PDF16_S6_SD_SC_SA_
    .private_segment_fixed_size: 0
    .sgpr_count:     35
    .sgpr_spill_count: 0
    .symbol:         _Z5k_gcnILi1EEvPKvPK15HIP_vector_typeIiLj2EEPfPKiS8_PKfPKDF16_SA_SA_SA_SA_S6_PDF16_S6_SD_SC_SA_.kd
    .uniform_work_group_size: 1
    .uses_dynamic_stack: false
    .vgpr_count:     72
    .vgpr_spill_count: 0
    .wavefront_size: 64
  - .agpr_count:     0
    .args:
      - .actual_access:  read_only
        .address_space:  global
        .offset:         0
        .size:           8
        .value_kind:     global_buffer
      - .actual_access:  read_only
        .address_space:  global
        .offset:         8
        .size:           8
        .value_kind:     global_buffer
      - .actual_access:  read_only
        .address_space:  global
        .offset:         16
        .size:           8
        .value_kind:     global_buffer
      - .actual_access:  read_only
        .address_space:  global
        .offset:         24
        .size:           8
        .value_kind:     global_buffer
      - .actual_access:  read_only
        .address_space:  global
        .offset:         32
        .size:           8
        .value_kind:     global_buffer
      - .actual_access:  read_only
        .address_space:  global
        .offset:         40
        .size:           8
        .value_kind:     global_buffer
      - .actual_access:  read_only
        .address_space:  global
        .offset:         48
        .size:           8
        .value_kind:     global_buffer
      - .actual_access:  read_only
        .address_space:  global
        .offset:         56
        .size:           8
        .value_kind:     global_buffer
      - .actual_access:  read_only
        .address_space:  global
        .offset:         64
        .size:           8
        .value_kind:     global_buffer
      - .actual_access:  read_only
        .address_space:  global
        .offset:         72
        .size:           8
        .value_kind:     global_buffer
      - .actual_access:  read_only
        .address_space:  global
        .offset:         80
        .size:           8
        .value_kind:     global_buffer
      - .actual_access:  read_only
        .address_space:  global
        .offset:         88
        .size:           8
        .value_kind:     global_buffer
      - .actual_access:  write_only
        .address_space:  global
        .offset:         96
        .size:           8
        .value_kind:     global_buffer
      - .address_space:  global
        .offset:         104
        .size:           8
        .value_kind:     global_buffer
      - .actual_access:  read_only
        .address_space:  global
        .offset:         112
        .size:           8
        .value_kind:     global_buffer
      - .actual_access:  read_only
        .address_space:  global
        .offset:         120
        .size:           8
        .value_kind:     global_buffer
      - .actual_access:  read_only
        .address_space:  global
        .offset:         128
        .size:           8
        .value_kind:     global_buffer
      - .offset:         136
        .size:           4
        .value_kind:     hidden_block_count_x
      - .offset:         140
        .size:           4
        .value_kind:     hidden_block_count_y
      - .offset:         144
        .size:           4
        .value_kind:     hidden_block_count_z
      - .offset:         148
        .size:           2
        .value_kind:     hidden_group_size_x
      - .offset:         150
        .size:           2
        .value_kind:     hidden_group_size_y
      - .offset:         152
        .size:           2
        .value_kind:     hidden_group_size_z
      - .offset:         154
        .size:           2
        .value_kind:     hidden_remainder_x
      - .offset:         156
        .size:           2
        .value_kind:     hidden_remainder_y
      - .offset:         158
        .size:           2
        .value_kind:     hidden_remainder_z
      - .offset:         176
        .size:           8
        .value_kind:     hidden_global_offset_x
      - .offset:         184
        .size:           8
        .value_kind:     hidden_global_offset_y
      - .offset:         192
        .size:           8
        .value_kind:     hidden_global_offset_z
      - .offset:         200
        .size:           2
        .value_kind:     hidden_grid_dims
    .group_segment_fixed_size: 32000
    .kernarg_segment_align: 8
    .kernarg_segment_size: 392
    .language:       OpenCL C
    .language_version:
      - 2
      - 0
    .max_flat_workgroup_size: 256
    .name:           _Z5k_gcnILi2EEvPKvPK15HIP_vector_typeIiLj2EEPfPKiS8_PKfPKDF16_SA_SA_SA_SA_S6_PDF16_S6_SD_SC_SA_
    .private_segment_fixed_size: 0
    .sgpr_count:     36
    .sgpr_spill_count: 0
    .symbol:         _Z5k_gcnILi2EEvPKvPK15HIP_vector_typeIiLj2EEPfPKiS8_PKfPKDF16_SA_SA_SA_SA_S6_PDF16_S6_SD_SC_SA_.kd
    .uniform_work_group_size: 1
    .uses_dynamic_stack: false
    .vgpr_count:     128
    .vgpr_spill_count: 0
    .wavefront_size: 64
  - .agpr_count:     0
    .args:
      - .actual_access:  read_only
        .address_space:  global
        .offset:         0
        .size:           8
        .value_kind:     global_buffer
      - .actual_access:  read_only
        .address_space:  global
        .offset:         8
        .size:           8
        .value_kind:     global_buffer
      - .actual_access:  read_only
        .address_space:  global
        .offset:         16
        .size:           8
        .value_kind:     global_buffer
      - .actual_access:  read_only
        .address_space:  global
        .offset:         24
        .size:           8
        .value_kind:     global_buffer
      - .actual_access:  write_only
        .address_space:  global
        .offset:         32
        .size:           8
        .value_kind:     global_buffer
      - .actual_access:  read_only
        .address_space:  global
        .offset:         40
        .size:           8
        .value_kind:     global_buffer
      - .actual_access:  read_only
        .address_space:  global
        .offset:         48
        .size:           8
        .value_kind:     global_buffer
      - .actual_access:  read_only
        .address_space:  global
        .offset:         56
        .size:           8
        .value_kind:     global_buffer
      - .actual_access:  read_only
        .address_space:  global
        .offset:         64
        .size:           8
        .value_kind:     global_buffer
      - .actual_access:  read_only
        .address_space:  global
        .offset:         72
        .size:           8
        .value_kind:     global_buffer
      - .actual_access:  read_only
        .address_space:  global
        .offset:         80
        .size:           8
        .value_kind:     global_buffer
      - .actual_access:  read_only
        .address_space:  global
        .offset:         88
        .size:           8
        .value_kind:     global_buffer
      - .actual_access:  write_only
        .address_space:  global
        .offset:         96
        .size:           8
        .value_kind:     global_buffer
    .group_segment_fixed_size: 9216
    .kernarg_segment_align: 8
    .kernarg_segment_size: 104
    .language:       OpenCL C
    .language_version:
      - 2
      - 0
    .max_flat_workgroup_size: 512
    .name:           _Z6k_lstmILi256ELi10ELb1ELb0EEvPKDF16_S1_S1_PKfPDF16_S1_S1_S1_S3_S3_S3_PfS5_
    .private_segment_fixed_size: 0
    .sgpr_count:     37
    .sgpr_spill_count: 0
    .symbol:         _Z6k_lstmILi256ELi10ELb1ELb0EEvPKDF16_S1_S1_PKfPDF16_S1_S1_S1_S3_S3_S3_PfS5_.kd
    .uniform_work_group_size: 1
    .uses_dynamic_stack: false
    .vgpr_count:     256
    .vgpr_spill_count: 0
    .wavefront_size: 64
  - .agpr_count:     0
    .args:
      - .actual_access:  read_only
        .address_space:  global
        .offset:         0
        .size:           8
        .value_kind:     global_buffer
      - .actual_access:  read_only
        .address_space:  global
        .offset:         8
        .size:           8
        .value_kind:     global_buffer
      - .actual_access:  read_only
        .address_space:  global
        .offset:         16
        .size:           8
        .value_kind:     global_buffer
      - .actual_access:  read_only
        .address_space:  global
        .offset:         24
        .size:           8
        .value_kind:     global_buffer
      - .actual_access:  read_only
        .address_space:  global
        .offset:         32
        .size:           8
        .value_kind:     global_buffer
      - .actual_access:  read_only
        .address_space:  global
        .offset:         40
        .size:           8
        .value_kind:     global_buffer
      - .actual_access:  read_only
        .address_space:  global
        .offset:         48
        .size:           8
        .value_kind:     global_buffer
      - .actual_access:  read_only
        .address_space:  global
        .offset:         56
        .size:           8
        .value_kind:     global_buffer
      - .actual_access:  read_only
        .address_space:  global
        .offset:         64
        .size:           8
        .value_kind:     global_buffer
      - .actual_access:  read_only
        .address_space:  global
        .offset:         72
        .size:           8
        .value_kind:     global_buffer
      - .actual_access:  read_only
        .address_space:  global
        .offset:         80
        .size:           8
        .value_kind:     global_buffer
      - .actual_access:  write_only
        .address_space:  global
        .offset:         88
        .size:           8
        .value_kind:     global_buffer
      - .actual_access:  read_only
        .address_space:  global
        .offset:         96
        .size:           8
        .value_kind:     global_buffer
    .group_segment_fixed_size: 0
    .kernarg_segment_align: 8
    .kernarg_segment_size: 104
    .language:       OpenCL C
    .language_version:
      - 2
      - 0
    .max_flat_workgroup_size: 512
    .name:           _Z6k_lstmILi128ELi8ELb0ELb1EEvPKDF16_S1_S1_PKfPDF16_S1_S1_S1_S3_S3_S3_PfS5_
    .private_segment_fixed_size: 0
    .sgpr_count:     46
    .sgpr_spill_count: 0
    .symbol:         _Z6k_lstmILi128ELi8ELb0ELb1EEvPKDF16_S1_S1_PKfPDF16_S1_S1_S1_S3_S3_S3_PfS5_.kd
    .uniform_work_group_size: 1
    .uses_dynamic_stack: false
    .vgpr_count:     256
    .vgpr_spill_count: 0
    .wavefront_size: 64
